# speedup vs baseline: 1.0101x; 1.0021x over previous
amdhsa.kernels:
  - .agpr_count:     0
    .args:
      - .actual_access:  read_only
        .address_space:  global
        .offset:         0
        .size:           8
        .value_kind:     global_buffer
      - .actual_access:  write_only
        .address_space:  global
        .offset:         8
        .size:           8
        .value_kind:     global_buffer
    .group_segment_fixed_size: 0
    .kernarg_segment_align: 8
    .kernarg_segment_size: 16
    .language:       OpenCL C
    .language_version:
      - 2
      - 0
    .max_flat_workgroup_size: 256
    .name:           _Z13prep_x_kernelPKfP15HIP_vector_typeIjLj4EE
    .private_segment_fixed_size: 0
    .sgpr_count:     23
    .sgpr_spill_count: 0
    .symbol:         _Z13prep_x_kernelPKfP15HIP_vector_typeIjLj4EE.kd
    .uniform_work_group_size: 1
    .uses_dynamic_stack: false
    .vgpr_count:     36
    .vgpr_spill_count: 0
    .wavefront_size: 64
  - .agpr_count:     0
    .args:
      - .actual_access:  read_only
        .address_space:  global
        .offset:         0
        .size:           8
        .value_kind:     global_buffer
      - .actual_access:  write_only
        .address_space:  global
        .offset:         8
        .size:           8
        .value_kind:     global_buffer
      - .offset:         16
        .size:           4
        .value_kind:     by_value
      - .offset:         20
        .size:           4
        .value_kind:     by_value
      - .offset:         24
        .size:           4
        .value_kind:     by_value
      - .offset:         28
        .size:           4
        .value_kind:     by_value
    .group_segment_fixed_size: 0
    .kernarg_segment_align: 8
    .kernarg_segment_size: 32
    .language:       OpenCL C
    .language_version:
      - 2
      - 0
    .max_flat_workgroup_size: 256
    .name:           _Z13prep_w_kernelPKfP15HIP_vector_typeIjLj4EEiiii
    .private_segment_fixed_size: 0
    .sgpr_count:     15
    .sgpr_spill_count: 0
    .symbol:         _Z13prep_w_kernelPKfP15HIP_vector_typeIjLj4EEiiii.kd
    .uniform_work_group_size: 1
    .uses_dynamic_stack: false
    .vgpr_count:     34
    .vgpr_spill_count: 0
    .wavefront_size: 64
  - .agpr_count:     0
    .args:
      - .actual_access:  write_only
        .address_space:  global
        .offset:         0
        .size:           8
        .value_kind:     global_buffer
    .group_segment_fixed_size: 0
    .kernarg_segment_align: 8
    .kernarg_segment_size: 8
    .language:       OpenCL C
    .language_version:
      - 2
      - 0
    .max_flat_workgroup_size: 256
    .name:           _Z18zero_border_kernelP15HIP_vector_typeIjLj4EE
    .private_segment_fixed_size: 0
    .sgpr_count:     12
    .sgpr_spill_count: 0
    .symbol:         _Z18zero_border_kernelP15HIP_vector_typeIjLj4EE.kd
    .uniform_work_group_size: 1
    .uses_dynamic_stack: false
    .vgpr_count:     6
    .vgpr_spill_count: 0
    .wavefront_size: 64
  - .agpr_count:     0
    .args:
      - .actual_access:  read_only
        .address_space:  global
        .offset:         0
        .size:           8
        .value_kind:     global_buffer
      - .address_space:  global
        .offset:         8
        .size:           8
        .value_kind:     global_buffer
      - .actual_access:  read_only
        .address_space:  global
        .offset:         16
        .size:           8
        .value_kind:     global_buffer
      - .actual_access:  read_only
        .address_space:  global
        .offset:         24
        .size:           8
        .value_kind:     global_buffer
      - .actual_access:  read_only
        .address_space:  global
        .offset:         32
        .size:           8
        .value_kind:     global_buffer
      - .actual_access:  write_only
        .address_space:  global
        .offset:         40
        .size:           8
        .value_kind:     global_buffer
    .group_segment_fixed_size: 154880
    .kernarg_segment_align: 8
    .kernarg_segment_size: 48
    .language:       OpenCL C
    .language_version:
      - 2
      - 0
    .max_flat_workgroup_size: 512
    .name:           _Z12conv1_kernelPKfPK15HIP_vector_typeIjLj4EES0_S0_S0_PDF16_
    .private_segment_fixed_size: 0
    .sgpr_count:     46
    .sgpr_spill_count: 0
    .symbol:         _Z12conv1_kernelPKfPK15HIP_vector_typeIjLj4EES0_S0_S0_PDF16_.kd
    .uniform_work_group_size: 1
    .uses_dynamic_stack: false
    .vgpr_count:     256
    .vgpr_spill_count: 0
    .wavefront_size: 64
  - .agpr_count:     0
    .args:
      - .actual_access:  read_only
        .address_space:  global
        .offset:         0
        .size:           8
        .value_kind:     global_buffer
      - .actual_access:  read_only
        .address_space:  global
        .offset:         8
        .size:           8
        .value_kind:     global_buffer
      - .actual_access:  read_only
        .address_space:  global
        .offset:         16
        .size:           8
        .value_kind:     global_buffer
      - .actual_access:  write_only
        .address_space:  global
        .offset:         24
        .size:           8
        .value_kind:     global_buffer
      - .actual_access:  write_only
        .address_space:  global
        .offset:         32
        .size:           8
        .value_kind:     global_buffer
    .group_segment_fixed_size: 116480
    .kernarg_segment_align: 8
    .kernarg_segment_size: 40
    .language:       OpenCL C
    .language_version:
      - 2
      - 0
    .max_flat_workgroup_size: 512
    .name:           _Z12conv3_kernelPK15HIP_vector_typeIjLj4EES2_PKfPfS5_
    .private_segment_fixed_size: 0
    .sgpr_count:     22
    .sgpr_spill_count: 0
    .symbol:         _Z12conv3_kernelPK15HIP_vector_typeIjLj4EES2_PKfPfS5_.kd
    .uniform_work_group_size: 1
    .uses_dynamic_stack: false
    .vgpr_count:     122
    .vgpr_spill_count: 0
    .wavefront_size: 64
  - .agpr_count:     0
    .args:
      - .actual_access:  read_only
        .address_space:  global
        .offset:         0
        .size:           8
        .value_kind:     global_buffer
      - .actual_access:  read_only
        .address_space:  global
        .offset:         8
        .size:           8
        .value_kind:     global_buffer
      - .actual_access:  write_only
        .address_space:  global
        .offset:         16
        .size:           8
        .value_kind:     global_buffer
      - .address_space:  global
        .offset:         24
        .size:           8
        .value_kind:     global_buffer
    .group_segment_fixed_size: 32768
    .kernarg_segment_align: 8
    .kernarg_segment_size: 32
    .language:       OpenCL C
    .language_version:
      - 2
      - 0
    .max_flat_workgroup_size: 256
    .name:           _Z15nms_hist_kernelPKfS0_PjS1_
    .private_segment_fixed_size: 0
    .sgpr_count:     102
    .sgpr_spill_count: 0
    .symbol:         _Z15nms_hist_kernelPKfS0_PjS1_.kd
    .uniform_work_group_size: 1
    .uses_dynamic_stack: false
    .vgpr_count:     128
    .vgpr_spill_count: 0
    .wavefront_size: 64
  - .agpr_count:     0
    .args:
      - .actual_access:  read_only
        .address_space:  global
        .offset:         0
        .size:           8
        .value_kind:     global_buffer
      - .actual_access:  write_only
        .address_space:  global
        .offset:         8
        .size:           8
        .value_kind:     global_buffer
    .group_segment_fixed_size: 4096
    .kernarg_segment_align: 8
    .kernarg_segment_size: 16
    .language:       OpenCL C
    .language_version:
      - 2
      - 0
    .max_flat_workgroup_size: 1024
    .name:           _Z17select_bin_kernelPKjPi
    .private_segment_fixed_size: 0
    .sgpr_count:     23
    .sgpr_spill_count: 0
    .symbol:         _Z17select_bin_kernelPKjPi.kd
    .uniform_work_group_size: 1
    .uses_dynamic_stack: false
    .vgpr_count:     13
    .vgpr_spill_count: 0
    .wavefront_size: 64
  - .agpr_count:     0
    .args:
      - .actual_access:  read_only
        .address_space:  global
        .offset:         0
        .size:           8
        .value_kind:     global_buffer
      - .actual_access:  read_only
        .address_space:  global
        .offset:         8
        .size:           8
        .value_kind:     global_buffer
      - .address_space:  global
        .offset:         16
        .size:           8
        .value_kind:     global_buffer
      - .actual_access:  write_only
        .address_space:  global
        .offset:         24
        .size:           8
        .value_kind:     global_buffer
    .group_segment_fixed_size: 2052
    .kernarg_segment_align: 8
    .kernarg_segment_size: 32
    .language:       OpenCL C
    .language_version:
      - 2
      - 0
    .max_flat_workgroup_size: 512
    .name:           _Z14collect_kernelPKjS0_PiS1_
    .private_segment_fixed_size: 0
    .sgpr_count:     70
    .sgpr_spill_count: 0
    .symbol:         _Z14collect_kernelPKjS0_PiS1_.kd
    .uniform_work_group_size: 1
    .uses_dynamic_stack: false
    .vgpr_count:     34
    .vgpr_spill_count: 0
    .wavefront_size: 64
  - .agpr_count:     0
    .args:
      - .actual_access:  read_only
        .address_space:  global
        .offset:         0
        .size:           8
        .value_kind:     global_buffer
      - .actual_access:  read_only
        .address_space:  global
        .offset:         8
        .size:           8
        .value_kind:     global_buffer
      - .actual_access:  read_only
        .address_space:  global
        .offset:         16
        .size:           8
        .value_kind:     global_buffer
      - .actual_access:  read_only
        .address_space:  global
        .offset:         24
        .size:           8
        .value_kind:     global_buffer
      - .actual_access:  write_only
        .address_space:  global
        .offset:         32
        .size:           8
        .value_kind:     global_buffer
    .group_segment_fixed_size: 49664
    .kernarg_segment_align: 8
    .kernarg_segment_size: 40
    .language:       OpenCL C
    .language_version:
      - 2
      - 0
    .max_flat_workgroup_size: 1024
    .name:           _Z11rank_kernelPKfS0_PKiS2_Pi
    .private_segment_fixed_size: 0
    .sgpr_count:     23
    .sgpr_spill_count: 0
    .symbol:         _Z11rank_kernelPKfS0_PKiS2_Pi.kd
    .uniform_work_group_size: 1
    .uses_dynamic_stack: false
    .vgpr_count:     12
    .vgpr_spill_count: 0
    .wavefront_size: 64
  - .agpr_count:     0
    .args:
      - .actual_access:  read_only
        .address_space:  global
        .offset:         0
        .size:           8
        .value_kind:     global_buffer
      - .actual_access:  read_only
        .address_space:  global
        .offset:         8
        .size:           8
        .value_kind:     global_buffer
      - .actual_access:  write_only
        .address_space:  global
        .offset:         16
        .size:           8
        .value_kind:     global_buffer
      - .actual_access:  write_only
        .address_space:  global
        .offset:         24
        .size:           8
        .value_kind:     global_buffer
    .group_segment_fixed_size: 0
    .kernarg_segment_align: 8
    .kernarg_segment_size: 32
    .language:       OpenCL C
    .language_version:
      - 2
      - 0
    .max_flat_workgroup_size: 256
    .name:           _Z15prep_kvw_kernelPKfS0_PDF16_S1_
    .private_segment_fixed_size: 0
    .sgpr_count:     14
    .sgpr_spill_count: 0
    .symbol:         _Z15prep_kvw_kernelPKfS0_PDF16_S1_.kd
    .uniform_work_group_size: 1
    .uses_dynamic_stack: false
    .vgpr_count:     7
    .vgpr_spill_count: 0
    .wavefront_size: 64
  - .agpr_count:     0
    .args:
      - .actual_access:  read_only
        .address_space:  global
        .offset:         0
        .size:           8
        .value_kind:     global_buffer
      - .actual_access:  read_only
        .address_space:  global
        .offset:         8
        .size:           8
        .value_kind:     global_buffer
      - .actual_access:  read_only
        .address_space:  global
        .offset:         16
        .size:           8
        .value_kind:     global_buffer
      - .actual_access:  read_only
        .address_space:  global
        .offset:         24
        .size:           8
        .value_kind:     global_buffer
      - .actual_access:  write_only
        .address_space:  global
        .offset:         32
        .size:           8
        .value_kind:     global_buffer
    .group_segment_fixed_size: 67856
    .kernarg_segment_align: 8
    .kernarg_segment_size: 40
    .language:       OpenCL C
    .language_version:
      - 2
      - 0
    .max_flat_workgroup_size: 448
    .name:           _Z17cross_attn_kernelPKDF16_S0_S0_S0_Pf
    .private_segment_fixed_size: 0
    .sgpr_count:     26
    .sgpr_spill_count: 0
    .symbol:         _Z17cross_attn_kernelPKDF16_S0_S0_S0_Pf.kd
    .uniform_work_group_size: 1
    .uses_dynamic_stack: false
    .vgpr_count:     74
    .vgpr_spill_count: 0
    .wavefront_size: 64
  - .agpr_count:     0
    .args:
      - .offset:         0
        .size:           424
        .value_kind:     by_value
      - .offset:         424
        .size:           88
        .value_kind:     by_value
    .group_segment_fixed_size: 137216
    .kernarg_segment_align: 8
    .kernarg_segment_size: 512
    .language:       OpenCL C
    .language_version:
      - 2
      - 0
    .max_flat_workgroup_size: 512
    .name:           _Z12tailA_kernel5TailP3KvP
    .private_segment_fixed_size: 0
    .sgpr_count:     44
    .sgpr_spill_count: 0
    .symbol:         _Z12tailA_kernel5TailP3KvP.kd
    .uniform_work_group_size: 1
    .uses_dynamic_stack: false
    .vgpr_count:     200
    .vgpr_spill_count: 0
    .wavefront_size: 64
  - .agpr_count:     0
    .args:
      - .offset:         0
        .size:           424
        .value_kind:     by_value
      - .offset:         424
        .size:           88
        .value_kind:     by_value
    .group_segment_fixed_size: 146592
    .kernarg_segment_align: 8
    .kernarg_segment_size: 512
    .language:       OpenCL C
    .language_version:
      - 2
      - 0
    .max_flat_workgroup_size: 512
    .name:           _Z12tailB_kernel5TailP3KvP
    .private_segment_fixed_size: 0
    .sgpr_count:     44
    .sgpr_spill_count: 0
    .symbol:         _Z12tailB_kernel5TailP3KvP.kd
    .uniform_work_group_size: 1
    .uses_dynamic_stack: false
    .vgpr_count:     216
    .vgpr_spill_count: 0
    .wavefront_size: 64
  - .agpr_count:     0
    .args:
      - .offset:         0
        .size:           424
        .value_kind:     by_value
    .group_segment_fixed_size: 36896
    .kernarg_segment_align: 8
    .kernarg_segment_size: 424
    .language:       OpenCL C
    .language_version:
      - 2
      - 0
    .max_flat_workgroup_size: 512
    .name:           _Z12tailC_kernel5TailP
    .private_segment_fixed_size: 0
    .sgpr_count:     58
    .sgpr_spill_count: 0
    .symbol:         _Z12tailC_kernel5TailP.kd
    .uniform_work_group_size: 1
    .uses_dynamic_stack: false
    .vgpr_count:     115
    .vgpr_spill_count: 0
    .wavefront_size: 64
  - .agpr_count:     0
    .args:
      - .offset:         0
        .size:           344
        .value_kind:     by_value
    .group_segment_fixed_size: 0
    .kernarg_segment_align: 8
    .kernarg_segment_size: 344
    .language:       OpenCL C
    .language_version:
      - 2
      - 0
    .max_flat_workgroup_size: 256
    .name:           _Z15prep_all_kernel5PrepP
    .private_segment_fixed_size: 0
    .sgpr_count:     31
    .sgpr_spill_count: 0
    .symbol:         _Z15prep_all_kernel5PrepP.kd
    .uniform_work_group_size: 1
    .uses_dynamic_stack: false
    .vgpr_count:     39
    .vgpr_spill_count: 0
    .wavefront_size: 64
  - .agpr_count:     0
    .args:
      - .actual_access:  read_only
        .address_space:  global
        .offset:         0
        .size:           8
        .value_kind:     global_buffer
      - .actual_access:  read_only
        .address_space:  global
        .offset:         8
        .size:           8
        .value_kind:     global_buffer
      - .actual_access:  read_only
        .address_space:  global
        .offset:         16
        .size:           8
        .value_kind:     global_buffer
      - .actual_access:  read_only
        .address_space:  global
        .offset:         24
        .size:           8
        .value_kind:     global_buffer
      - .actual_access:  read_only
        .address_space:  global
        .offset:         32
        .size:           8
        .value_kind:     global_buffer
      - .actual_access:  write_only
        .address_space:  global
        .offset:         40
        .size:           8
        .value_kind:     global_buffer
      - .actual_access:  read_only
        .address_space:  global
        .offset:         48
        .size:           8
        .value_kind:     global_buffer
      - .actual_access:  read_only
        .address_space:  global
        .offset:         56
        .size:           8
        .value_kind:     global_buffer
    .group_segment_fixed_size: 130304
    .kernarg_segment_align: 8
    .kernarg_segment_size: 64
    .language:       OpenCL C
    .language_version:
      - 2
      - 0
    .max_flat_workgroup_size: 512
    .name:           _Z11conv_kernelILi8ELi128ELi0EEvPK15HIP_vector_typeIjLj4EES3_PKfS5_S5_PDF16_PfS7_
    .private_segment_fixed_size: 0
    .sgpr_count:     30
    .sgpr_spill_count: 0
    .symbol:         _Z11conv_kernelILi8ELi128ELi0EEvPK15HIP_vector_typeIjLj4EES3_PKfS5_S5_PDF16_PfS7_.kd
    .uniform_work_group_size: 1
    .uses_dynamic_stack: false
    .vgpr_count:     256
    .vgpr_spill_count: 0
    .wavefront_size: 64
